# P8 K-loop per-half specialisation: leading half defers its vmcnt waits to the end of the next MFMA block, trailing half issues its SP2 stage DMAs one interval earlier (in the SP1 MFMA block)
# baseline (speedup 1.0000x reference)
.LBB0_899:
	s_ashr_i32 s31, s30, 31
	s_lshl_b64 s[2:3], s[30:31], 19
	s_add_u32 s38, s6, s2
	s_addc_u32 s39, s7, s3
	s_and_b64 s[2:3], s[26:27], exec
	v_readlane_b32 s2, v251, 50
	s_cselect_b32 s29, s39, s53
	s_cselect_b32 s31, s38, s52
	s_add_u32 s40, s2, s36
	v_readlane_b32 s2, v251, 51
	s_addc_u32 s41, s2, s37
	s_and_b64 s[2:3], s[26:27], exec
	s_cselect_b32 s35, s41, s51
	s_cselect_b32 s43, s40, s50
	s_cmpk_gt_i32 s48, 0x80
	s_cselect_b64 s[48:49], -1, 0
	s_add_u32 s70, s50, 0x80000
	s_addc_u32 s71, s51, 0
	v_mov_b32_e32 v68, v66
	v_mov_b32_e32 v69, v66
	s_add_u32 s50, s52, 0x40080
	v_mov_b32_e32 v67, v66
	v_mov_b32_e32 v134, 0
	v_mov_b64_e32 v[72:73], v[68:69]
	v_mov_b64_e32 v[76:77], v[68:69]
	v_mov_b64_e32 v[88:89], v[68:69]
	v_mov_b64_e32 v[92:93], v[68:69]
	v_mov_b64_e32 v[104:105], v[68:69]
	v_mov_b64_e32 v[108:109], v[68:69]
	v_mov_b64_e32 v[120:121], v[68:69]
	v_mov_b64_e32 v[124:125], v[68:69]
	v_mov_b64_e32 v[80:81], v[68:69]
	v_mov_b64_e32 v[84:85], v[68:69]
	v_mov_b64_e32 v[96:97], v[68:69]
	v_mov_b64_e32 v[100:101], v[68:69]
	v_mov_b64_e32 v[112:113], v[68:69]
	v_mov_b64_e32 v[116:117], v[68:69]
	v_mov_b64_e32 v[128:129], v[68:69]
	v_mov_b64_e32 v[132:133], v[68:69]
	s_addc_u32 s51, s53, 0
	s_mov_b32 s72, -2
	v_cndmask_b32_e64 v225, 0, 1, s[48:49]
	v_mov_b64_e32 v[70:71], v[66:67]
	v_mov_b64_e32 v[74:75], v[66:67]
	v_mov_b64_e32 v[86:87], v[66:67]
	v_mov_b64_e32 v[90:91], v[66:67]
	v_mov_b64_e32 v[102:103], v[66:67]
	v_mov_b64_e32 v[106:107], v[66:67]
	v_mov_b64_e32 v[118:119], v[66:67]
	v_mov_b64_e32 v[122:123], v[66:67]
	v_mov_b64_e32 v[78:79], v[66:67]
	v_mov_b64_e32 v[82:83], v[66:67]
	v_mov_b64_e32 v[94:95], v[66:67]
	v_mov_b64_e32 v[98:99], v[66:67]
	v_mov_b64_e32 v[110:111], v[66:67]
	v_mov_b64_e32 v[114:115], v[66:67]
	v_mov_b64_e32 v[126:127], v[66:67]
	v_mov_b64_e32 v[130:131], v[66:67]
	v_mov_b32_e32 v135, v134
	v_mov_b32_e32 v136, v134
	v_mov_b32_e32 v137, v134
	v_mov_b32_e32 v138, v134
	v_mov_b32_e32 v139, v134
	v_mov_b32_e32 v140, v134
	v_mov_b32_e32 v141, v134
	v_mov_b32_e32 v150, v134
	v_mov_b32_e32 v151, v134
	v_mov_b32_e32 v152, v134
	v_mov_b32_e32 v153, v134
	v_mov_b32_e32 v154, v134
	v_mov_b32_e32 v155, v134
	v_mov_b32_e32 v156, v134
	v_mov_b32_e32 v157, v134
	v_mov_b32_e32 v166, v134
	v_mov_b32_e32 v167, v134
	v_mov_b32_e32 v168, v134
	v_mov_b32_e32 v169, v134
	v_mov_b32_e32 v170, v134
	v_mov_b32_e32 v171, v134
	v_mov_b32_e32 v172, v134
	v_mov_b32_e32 v173, v134
	v_mov_b32_e32 v174, v134
	v_mov_b32_e32 v175, v134
	v_mov_b32_e32 v176, v134
	v_mov_b32_e32 v177, v134
	v_mov_b32_e32 v178, v134
	v_mov_b32_e32 v179, v134
	v_mov_b32_e32 v180, v134
	v_mov_b32_e32 v181, v134
	v_mov_b32_e32 v142, v134
	v_mov_b32_e32 v143, v134
	v_mov_b32_e32 v144, v134
	v_mov_b32_e32 v145, v134
	v_mov_b32_e32 v146, v134
	v_mov_b32_e32 v147, v134
	v_mov_b32_e32 v148, v134
	v_mov_b32_e32 v149, v134
	v_mov_b32_e32 v158, v134
	v_mov_b32_e32 v159, v134
	v_mov_b32_e32 v160, v134
	v_mov_b32_e32 v161, v134
	v_mov_b32_e32 v162, v134
	v_mov_b32_e32 v163, v134
	v_mov_b32_e32 v164, v134
	v_mov_b32_e32 v165, v134
	v_mov_b32_e32 v182, v134
	v_mov_b32_e32 v183, v134
	v_mov_b32_e32 v184, v134
	v_mov_b32_e32 v185, v134
	v_mov_b32_e32 v186, v134
	v_mov_b32_e32 v187, v134
	v_mov_b32_e32 v188, v134
	v_mov_b32_e32 v189, v134
	v_mov_b32_e32 v190, v134
	v_mov_b32_e32 v191, v134
	v_mov_b32_e32 v192, v134
	v_mov_b32_e32 v193, v134
	v_mov_b32_e32 v194, v134
	v_mov_b32_e32 v195, v134
	v_mov_b32_e32 v196, v134
	v_mov_b32_e32 v197, v134
	s_waitcnt vmcnt(0)
	s_cmp_eq_u64 s[14:15], 0
	s_cbranch_scc1 .Lp8t_901
	s_branch .LBB0_901

.LBB0_901:
	ds_read_b64_tr_b16 v[26:27], v207 offset:0
	ds_read_b64_tr_b16 v[28:29], v207 offset:1024
	ds_read_b64_tr_b16 v[30:31], v207 offset:8192
	ds_read_b64_tr_b16 v[32:33], v207 offset:9216
	ds_read_b64_tr_b16 v[18:19], v217 offset:0
	ds_read_b64_tr_b16 v[20:21], v217 offset:1024
	ds_read_b64_tr_b16 v[22:23], v217 offset:8192
	ds_read_b64_tr_b16 v[24:25], v217 offset:9216
	ds_read_b64_tr_b16 v[10:11], v214 offset:0
	ds_read_b64_tr_b16 v[12:13], v214 offset:1024
	ds_read_b64_tr_b16 v[14:15], v214 offset:8192
	ds_read_b64_tr_b16 v[16:17], v214 offset:9216
	ds_read_b64_tr_b16 v[2:3], v218 offset:0
	ds_read_b64_tr_b16 v[4:5], v218 offset:1024
	ds_read_b64_tr_b16 v[6:7], v218 offset:8192
	ds_read_b64_tr_b16 v[8:9], v218 offset:9216
	s_add_u32 s2, s50, 0xfffc0080
	s_addc_u32 s3, s51, -1
	s_cmp_eq_u32 s72, 12
	s_cselect_b32 s55, s29, s3
	s_cselect_b32 s54, s31, s2
	s_cselect_b32 s53, s35, s71
	s_cselect_b32 s52, s43, s70
	ds_read_b128 v[34:37], v223
	ds_read_b128 v[38:41], v223 offset:1024
	ds_read_b128 v[42:45], v223 offset:2048
	ds_read_b128 v[46:49], v223 offset:3072
	ds_read_b128 v[50:53], v223 offset:4096
	ds_read_b128 v[54:57], v223 offset:5120
	ds_read_b128 v[58:61], v223 offset:6144
	ds_read_b128 v[62:65], v223 offset:7168
	s_waitcnt lgkmcnt(0)
	s_barrier
	s_setprio 1
	s_waitcnt lgkmcnt(0)
	v_mfma_scale_f32_16x16x128_f8f6f4 v[194:197], v[26:33], v[34:41], v[194:197], v1, v1 op_sel_hi:[0,0,0]
	v_mfma_scale_f32_16x16x128_f8f6f4 v[190:193], v[18:25], v[34:41], v[190:193], v1, v1 op_sel_hi:[0,0,0]
	v_mfma_scale_f32_16x16x128_f8f6f4 v[186:189], v[26:33], v[42:49], v[186:189], v1, v1 op_sel_hi:[0,0,0]
	v_mfma_scale_f32_16x16x128_f8f6f4 v[182:185], v[18:25], v[42:49], v[182:185], v1, v1 op_sel_hi:[0,0,0]
	v_lshl_add_u64 v[68:69], s[50:51], 0, v[208:209]
	s_add_i32 m0, s17, 0xc000
	s_nop 0
	global_load_lds_dwordx4 v[68:69], off
	v_mfma_scale_f32_16x16x128_f8f6f4 v[162:165], v[26:33], v[50:57], v[162:165], v1, v1 op_sel_hi:[0,0,0]
	v_mfma_scale_f32_16x16x128_f8f6f4 v[158:161], v[18:25], v[50:57], v[158:161], v1, v1 op_sel_hi:[0,0,0]
	v_mfma_scale_f32_16x16x128_f8f6f4 v[146:149], v[26:33], v[58:65], v[146:149], v1, v1 op_sel_hi:[0,0,0]
	v_mfma_scale_f32_16x16x128_f8f6f4 v[142:145], v[18:25], v[58:65], v[142:145], v1, v1 op_sel_hi:[0,0,0]
	s_setprio 0
	s_setprio 1
	v_mfma_scale_f32_16x16x128_f8f6f4 v[178:181], v[10:17], v[34:41], v[178:181], v1, v1 op_sel_hi:[0,0,0]
	v_mfma_scale_f32_16x16x128_f8f6f4 v[174:177], v[2:9], v[34:41], v[174:177], v1, v1 op_sel_hi:[0,0,0]
	v_lshl_add_u64 v[68:69], s[50:51], 0, v[210:211]
	s_add_i32 m0, s17, 0xe000
	s_nop 0
	global_load_lds_dwordx4 v[68:69], off
	v_mfma_scale_f32_16x16x128_f8f6f4 v[170:173], v[10:17], v[42:49], v[170:173], v1, v1 op_sel_hi:[0,0,0]
	v_mfma_scale_f32_16x16x128_f8f6f4 v[166:169], v[2:9], v[42:49], v[166:169], v1, v1 op_sel_hi:[0,0,0]
	v_mfma_scale_f32_16x16x128_f8f6f4 v[154:157], v[10:17], v[50:57], v[154:157], v1, v1 op_sel_hi:[0,0,0]
	v_mfma_scale_f32_16x16x128_f8f6f4 v[150:153], v[2:9], v[50:57], v[150:153], v1, v1 op_sel_hi:[0,0,0]
	v_mfma_scale_f32_16x16x128_f8f6f4 v[138:141], v[10:17], v[58:65], v[138:141], v1, v1 op_sel_hi:[0,0,0]
	v_mfma_scale_f32_16x16x128_f8f6f4 v[134:137], v[2:9], v[58:65], v[134:137], v1, v1 op_sel_hi:[0,0,0]
	s_waitcnt vmcnt(8)
	s_setprio 0
	s_barrier
	s_mov_b32 m0, s19
	v_lshl_add_u64 v[68:69], s[52:53], 0, v[200:201]
	global_load_lds_dwordx4 v[68:69], off
	v_lshl_add_u64 v[212:213], s[52:53], 0, v[204:205]
	s_mov_b32 m0, s33
	v_lshl_add_u64 v[68:69], v[68:69], 0, s[4:5]
	global_load_lds_dwordx4 v[212:213], off
	s_mov_b32 m0, s45
	s_nop 0
	global_load_lds_dwordx4 v[68:69], off
	v_lshl_add_u64 v[68:69], v[212:213], 0, s[4:5]
	s_mov_b32 m0, s47
	v_lshl_add_u64 v[212:213], s[54:55], 0, v[202:203]
	global_load_lds_dwordx4 v[68:69], off
	s_andn2_b64 vcc, exec, s[48:49]
	s_cbranch_vccnz .Lhalfskip_p8a
	ds_read_b128 v[58:61], v223 offset:16384
	ds_read_b128 v[62:65], v223 offset:17408
	ds_read_b128 v[50:53], v223 offset:18432
	ds_read_b128 v[54:57], v223 offset:19456
	ds_read_b128 v[42:45], v223 offset:20480
	ds_read_b128 v[46:49], v223 offset:21504
	ds_read_b128 v[34:37], v223 offset:22528
	ds_read_b128 v[38:41], v223 offset:23552
.Lhalfskip_p8a:
	v_cmp_ne_u32_e64 s[2:3], 1, v225
	s_waitcnt lgkmcnt(0)
	s_barrier
	s_cbranch_vccnz .Lp8_skip_b
	s_setprio 1
	s_waitcnt lgkmcnt(0)
	v_mfma_scale_f32_16x16x128_f8f6f4 v[130:133], v[26:33], v[58:65], v[130:133], v1, v1 op_sel_hi:[0,0,0]
	v_mfma_scale_f32_16x16x128_f8f6f4 v[126:129], v[18:25], v[58:65], v[126:129], v1, v1 op_sel_hi:[0,0,0]
	v_mfma_scale_f32_16x16x128_f8f6f4 v[114:117], v[26:33], v[50:57], v[114:117], v1, v1 op_sel_hi:[0,0,0]
	v_mfma_scale_f32_16x16x128_f8f6f4 v[110:113], v[18:25], v[50:57], v[110:113], v1, v1 op_sel_hi:[0,0,0]
	v_mfma_scale_f32_16x16x128_f8f6f4 v[98:101], v[26:33], v[42:49], v[98:101], v1, v1 op_sel_hi:[0,0,0]
	v_mfma_scale_f32_16x16x128_f8f6f4 v[94:97], v[18:25], v[42:49], v[94:97], v1, v1 op_sel_hi:[0,0,0]
	v_mfma_scale_f32_16x16x128_f8f6f4 v[82:85], v[26:33], v[34:41], v[82:85], v1, v1 op_sel_hi:[0,0,0]
	v_mfma_scale_f32_16x16x128_f8f6f4 v[78:81], v[18:25], v[34:41], v[78:81], v1, v1 op_sel_hi:[0,0,0]
	s_setprio 0
	s_setprio 1
	v_mfma_scale_f32_16x16x128_f8f6f4 v[122:125], v[10:17], v[58:65], v[122:125], v1, v1 op_sel_hi:[0,0,0]
	v_mfma_scale_f32_16x16x128_f8f6f4 v[118:121], v[2:9], v[58:65], v[118:121], v1, v1 op_sel_hi:[0,0,0]
	v_mfma_scale_f32_16x16x128_f8f6f4 v[106:109], v[10:17], v[50:57], v[106:109], v1, v1 op_sel_hi:[0,0,0]
	v_lshl_add_u64 v[68:69], s[54:55], 0, v[198:199]
	s_mov_b32 m0, s17
	s_nop 0
	global_load_lds_dwordx4 v[68:69], off
	v_mfma_scale_f32_16x16x128_f8f6f4 v[102:105], v[2:9], v[50:57], v[102:105], v1, v1 op_sel_hi:[0,0,0]
	v_mfma_scale_f32_16x16x128_f8f6f4 v[90:93], v[10:17], v[42:49], v[90:93], v1, v1 op_sel_hi:[0,0,0]
	s_mov_b32 m0, s58
	s_nop 0
	global_load_lds_dwordx4 v[212:213], off
	v_mfma_scale_f32_16x16x128_f8f6f4 v[86:89], v[2:9], v[42:49], v[86:89], v1, v1 op_sel_hi:[0,0,0]
	v_mfma_scale_f32_16x16x128_f8f6f4 v[74:77], v[10:17], v[34:41], v[74:77], v1, v1 op_sel_hi:[0,0,0]
	v_mfma_scale_f32_16x16x128_f8f6f4 v[70:73], v[2:9], v[34:41], v[70:73], v1, v1 op_sel_hi:[0,0,0]
	s_waitcnt vmcnt(8)
	s_setprio 0
.LBB0_903:
	s_add_u32 s56, s52, 0x40000
	s_addc_u32 s57, s53, 0
	s_barrier
	ds_read_b64_tr_b16 v[26:27], v215 offset:0
	ds_read_b64_tr_b16 v[28:29], v215 offset:1024
	ds_read_b64_tr_b16 v[30:31], v215 offset:8192
	ds_read_b64_tr_b16 v[32:33], v215 offset:9216
	ds_read_b64_tr_b16 v[18:19], v219 offset:0
	ds_read_b64_tr_b16 v[20:21], v219 offset:1024
	ds_read_b64_tr_b16 v[22:23], v219 offset:8192
	ds_read_b64_tr_b16 v[24:25], v219 offset:9216
	ds_read_b64_tr_b16 v[10:11], v216 offset:0
	ds_read_b64_tr_b16 v[12:13], v216 offset:1024
	ds_read_b64_tr_b16 v[14:15], v216 offset:8192
	ds_read_b64_tr_b16 v[16:17], v216 offset:9216
	ds_read_b64_tr_b16 v[2:3], v220 offset:0
	ds_read_b64_tr_b16 v[4:5], v220 offset:1024
	ds_read_b64_tr_b16 v[6:7], v220 offset:8192
	ds_read_b64_tr_b16 v[8:9], v220 offset:9216
	s_add_u32 s54, s54, 0x40000
	s_addc_u32 s55, s55, 0
	ds_read_b128 v[34:37], v223 offset:32768
	ds_read_b128 v[38:41], v223 offset:33792
	ds_read_b128 v[42:45], v223 offset:34816
	ds_read_b128 v[46:49], v223 offset:35840
	ds_read_b128 v[50:53], v223 offset:36864
	ds_read_b128 v[54:57], v223 offset:37888
	ds_read_b128 v[58:61], v223 offset:38912
	ds_read_b128 v[62:65], v223 offset:39936
	s_waitcnt lgkmcnt(0)
	s_barrier
	s_setprio 1
	s_waitcnt lgkmcnt(0)
	v_mfma_scale_f32_16x16x128_f8f6f4 v[194:197], v[26:33], v[34:41], v[194:197], v1, v1 op_sel_hi:[0,0,0]
	v_mfma_scale_f32_16x16x128_f8f6f4 v[190:193], v[18:25], v[34:41], v[190:193], v1, v1 op_sel_hi:[0,0,0]
	v_mfma_scale_f32_16x16x128_f8f6f4 v[186:189], v[26:33], v[42:49], v[186:189], v1, v1 op_sel_hi:[0,0,0]
	v_mfma_scale_f32_16x16x128_f8f6f4 v[182:185], v[18:25], v[42:49], v[182:185], v1, v1 op_sel_hi:[0,0,0]
	s_mov_b32 m0, s59
	v_lshl_add_u64 v[226:227], s[54:55], 0, v[198:199]
	global_load_lds_dwordx4 v[226:227], off
	v_mfma_scale_f32_16x16x128_f8f6f4 v[162:165], v[26:33], v[50:57], v[162:165], v1, v1 op_sel_hi:[0,0,0]
	v_mfma_scale_f32_16x16x128_f8f6f4 v[158:161], v[18:25], v[50:57], v[158:161], v1, v1 op_sel_hi:[0,0,0]
	v_mfma_scale_f32_16x16x128_f8f6f4 v[146:149], v[26:33], v[58:65], v[146:149], v1, v1 op_sel_hi:[0,0,0]
	v_mfma_scale_f32_16x16x128_f8f6f4 v[142:145], v[18:25], v[58:65], v[142:145], v1, v1 op_sel_hi:[0,0,0]
	s_setprio 0
	s_setprio 1
	v_mfma_scale_f32_16x16x128_f8f6f4 v[178:181], v[10:17], v[34:41], v[178:181], v1, v1 op_sel_hi:[0,0,0]
	v_mfma_scale_f32_16x16x128_f8f6f4 v[174:177], v[2:9], v[34:41], v[174:177], v1, v1 op_sel_hi:[0,0,0]
	v_lshl_add_u64 v[226:227], s[54:55], 0, v[202:203]
	s_mov_b32 m0, s60
	s_nop 0
	global_load_lds_dwordx4 v[226:227], off
	v_mfma_scale_f32_16x16x128_f8f6f4 v[170:173], v[10:17], v[42:49], v[170:173], v1, v1 op_sel_hi:[0,0,0]
	v_mfma_scale_f32_16x16x128_f8f6f4 v[166:169], v[2:9], v[42:49], v[166:169], v1, v1 op_sel_hi:[0,0,0]
	v_mfma_scale_f32_16x16x128_f8f6f4 v[154:157], v[10:17], v[50:57], v[154:157], v1, v1 op_sel_hi:[0,0,0]
	v_mfma_scale_f32_16x16x128_f8f6f4 v[150:153], v[2:9], v[50:57], v[150:153], v1, v1 op_sel_hi:[0,0,0]
	v_mfma_scale_f32_16x16x128_f8f6f4 v[138:141], v[10:17], v[58:65], v[138:141], v1, v1 op_sel_hi:[0,0,0]
	v_mfma_scale_f32_16x16x128_f8f6f4 v[134:137], v[2:9], v[58:65], v[134:137], v1, v1 op_sel_hi:[0,0,0]
	s_waitcnt vmcnt(8)
	s_setprio 0
	s_barrier
	v_lshl_add_u64 v[226:227], s[56:57], 0, v[200:201]
	s_add_i32 m0, s17, 0x18000
	s_nop 0
	global_load_lds_dwordx4 v[226:227], off
	s_add_i32 m0, s17, 0x1a000
	v_lshl_add_u64 v[226:227], s[56:57], 0, v[204:205]
	global_load_lds_dwordx4 v[226:227], off
	s_add_u32 s52, s52, 0x40100
	s_addc_u32 s53, s53, 0
	v_lshl_add_u64 v[226:227], s[52:53], 0, v[200:201]
	s_add_i32 m0, s17, 0x1c000
	v_lshl_add_u64 v[68:69], v[68:69], 0, s[12:13]
	global_load_lds_dwordx4 v[226:227], off
	v_lshl_add_u64 v[226:227], s[52:53], 0, v[204:205]
	s_add_i32 m0, s17, 0x1e000
	s_nop 0
	global_load_lds_dwordx4 v[226:227], off
	s_and_b64 vcc, exec, s[2:3]
	s_cbranch_vccnz .Lhalfskip_p8b
	ds_read_b128 v[58:61], v223 offset:49152
	ds_read_b128 v[62:65], v223 offset:50176
	ds_read_b128 v[50:53], v223 offset:51200
	ds_read_b128 v[54:57], v223 offset:52224
	ds_read_b128 v[42:45], v223 offset:53248
	ds_read_b128 v[46:49], v223 offset:54272
	ds_read_b128 v[34:37], v223 offset:55296
	ds_read_b128 v[38:41], v223 offset:56320
.Lhalfskip_p8b:
	s_waitcnt lgkmcnt(0)
	s_barrier
	s_cbranch_vccnz .Lp8_skip_d
	s_setprio 1
	s_waitcnt lgkmcnt(0)
	v_mfma_scale_f32_16x16x128_f8f6f4 v[130:133], v[26:33], v[58:65], v[130:133], v1, v1 op_sel_hi:[0,0,0]
	v_mfma_scale_f32_16x16x128_f8f6f4 v[126:129], v[18:25], v[58:65], v[126:129], v1, v1 op_sel_hi:[0,0,0]
	v_mfma_scale_f32_16x16x128_f8f6f4 v[114:117], v[26:33], v[50:57], v[114:117], v1, v1 op_sel_hi:[0,0,0]
	v_mfma_scale_f32_16x16x128_f8f6f4 v[110:113], v[18:25], v[50:57], v[110:113], v1, v1 op_sel_hi:[0,0,0]
	v_mfma_scale_f32_16x16x128_f8f6f4 v[98:101], v[26:33], v[42:49], v[98:101], v1, v1 op_sel_hi:[0,0,0]
	v_mfma_scale_f32_16x16x128_f8f6f4 v[94:97], v[18:25], v[42:49], v[94:97], v1, v1 op_sel_hi:[0,0,0]
	v_mfma_scale_f32_16x16x128_f8f6f4 v[82:85], v[26:33], v[34:41], v[82:85], v1, v1 op_sel_hi:[0,0,0]
	v_mfma_scale_f32_16x16x128_f8f6f4 v[78:81], v[18:25], v[34:41], v[78:81], v1, v1 op_sel_hi:[0,0,0]
	s_setprio 0
	s_setprio 1
	v_mfma_scale_f32_16x16x128_f8f6f4 v[122:125], v[10:17], v[58:65], v[122:125], v1, v1 op_sel_hi:[0,0,0]
	v_mfma_scale_f32_16x16x128_f8f6f4 v[118:121], v[2:9], v[58:65], v[118:121], v1, v1 op_sel_hi:[0,0,0]
	v_mfma_scale_f32_16x16x128_f8f6f4 v[106:109], v[10:17], v[50:57], v[106:109], v1, v1 op_sel_hi:[0,0,0]
	s_mov_b32 m0, s62
	s_nop 0
	global_load_lds_dwordx4 v[68:69], off
	v_mfma_scale_f32_16x16x128_f8f6f4 v[102:105], v[2:9], v[50:57], v[102:105], v1, v1 op_sel_hi:[0,0,0]
	v_mfma_scale_f32_16x16x128_f8f6f4 v[90:93], v[10:17], v[42:49], v[90:93], v1, v1 op_sel_hi:[0,0,0]
	v_lshl_add_u64 v[68:69], v[212:213], 0, s[12:13]
	s_mov_b32 m0, s63
	s_nop 0
	global_load_lds_dwordx4 v[68:69], off
	v_mfma_scale_f32_16x16x128_f8f6f4 v[86:89], v[2:9], v[42:49], v[86:89], v1, v1 op_sel_hi:[0,0,0]
	v_mfma_scale_f32_16x16x128_f8f6f4 v[74:77], v[10:17], v[34:41], v[74:77], v1, v1 op_sel_hi:[0,0,0]
	v_mfma_scale_f32_16x16x128_f8f6f4 v[70:73], v[2:9], v[34:41], v[70:73], v1, v1 op_sel_hi:[0,0,0]
	s_waitcnt vmcnt(8)
	s_setprio 0
	s_branch .LBB0_900
.Lp8_skip_b:
	v_lshl_add_u64 v[68:69], s[54:55], 0, v[198:199]
	s_mov_b32 m0, s17
	s_nop 0
	global_load_lds_dwordx4 v[68:69], off
	s_mov_b32 m0, s58
	s_nop 0
	global_load_lds_dwordx4 v[212:213], off
	s_waitcnt vmcnt(8)
	s_branch .LBB0_903
.Lp8_skip_d:
	s_mov_b32 m0, s62
	s_nop 0
	global_load_lds_dwordx4 v[68:69], off
	v_lshl_add_u64 v[68:69], v[212:213], 0, s[12:13]
	s_mov_b32 m0, s63
	s_nop 0
	global_load_lds_dwordx4 v[68:69], off
	s_waitcnt vmcnt(8)
	s_branch .LBB0_900

.Lp8t_901:
	ds_read_b64_tr_b16 v[26:27], v207 offset:0
	ds_read_b64_tr_b16 v[28:29], v207 offset:1024
	ds_read_b64_tr_b16 v[30:31], v207 offset:8192
	ds_read_b64_tr_b16 v[32:33], v207 offset:9216
	ds_read_b64_tr_b16 v[18:19], v217 offset:0
	ds_read_b64_tr_b16 v[20:21], v217 offset:1024
	ds_read_b64_tr_b16 v[22:23], v217 offset:8192
	ds_read_b64_tr_b16 v[24:25], v217 offset:9216
	ds_read_b64_tr_b16 v[10:11], v214 offset:0
	ds_read_b64_tr_b16 v[12:13], v214 offset:1024
	ds_read_b64_tr_b16 v[14:15], v214 offset:8192
	ds_read_b64_tr_b16 v[16:17], v214 offset:9216
	ds_read_b64_tr_b16 v[2:3], v218 offset:0
	ds_read_b64_tr_b16 v[4:5], v218 offset:1024
	ds_read_b64_tr_b16 v[6:7], v218 offset:8192
	ds_read_b64_tr_b16 v[8:9], v218 offset:9216
	s_add_u32 s2, s50, 0xfffc0080
	s_addc_u32 s3, s51, -1
	s_cmp_eq_u32 s72, 12
	s_cselect_b32 s55, s29, s3
	s_cselect_b32 s54, s31, s2
	s_cselect_b32 s53, s35, s71
	s_cselect_b32 s52, s43, s70
	ds_read_b128 v[34:37], v223
	ds_read_b128 v[38:41], v223 offset:1024
	ds_read_b128 v[42:45], v223 offset:2048
	ds_read_b128 v[46:49], v223 offset:3072
	ds_read_b128 v[50:53], v223 offset:4096
	ds_read_b128 v[54:57], v223 offset:5120
	ds_read_b128 v[58:61], v223 offset:6144
	ds_read_b128 v[62:65], v223 offset:7168
	s_waitcnt vmcnt(6)
	s_waitcnt lgkmcnt(0)
	s_barrier
	s_setprio 1
	s_waitcnt lgkmcnt(0)
	v_mfma_scale_f32_16x16x128_f8f6f4 v[194:197], v[26:33], v[34:41], v[194:197], v1, v1 op_sel_hi:[0,0,0]
	v_mfma_scale_f32_16x16x128_f8f6f4 v[190:193], v[18:25], v[34:41], v[190:193], v1, v1 op_sel_hi:[0,0,0]
	v_mfma_scale_f32_16x16x128_f8f6f4 v[186:189], v[26:33], v[42:49], v[186:189], v1, v1 op_sel_hi:[0,0,0]
	v_mfma_scale_f32_16x16x128_f8f6f4 v[182:185], v[18:25], v[42:49], v[182:185], v1, v1 op_sel_hi:[0,0,0]
	v_lshl_add_u64 v[68:69], s[50:51], 0, v[208:209]
	s_add_i32 m0, s17, 0xc000
	s_nop 0
	global_load_lds_dwordx4 v[68:69], off
	v_mfma_scale_f32_16x16x128_f8f6f4 v[162:165], v[26:33], v[50:57], v[162:165], v1, v1 op_sel_hi:[0,0,0]
	v_mfma_scale_f32_16x16x128_f8f6f4 v[158:161], v[18:25], v[50:57], v[158:161], v1, v1 op_sel_hi:[0,0,0]
	v_mfma_scale_f32_16x16x128_f8f6f4 v[146:149], v[26:33], v[58:65], v[146:149], v1, v1 op_sel_hi:[0,0,0]
	v_mfma_scale_f32_16x16x128_f8f6f4 v[142:145], v[18:25], v[58:65], v[142:145], v1, v1 op_sel_hi:[0,0,0]
	s_setprio 0
	s_setprio 1
	v_mfma_scale_f32_16x16x128_f8f6f4 v[178:181], v[10:17], v[34:41], v[178:181], v1, v1 op_sel_hi:[0,0,0]
	v_mfma_scale_f32_16x16x128_f8f6f4 v[174:177], v[2:9], v[34:41], v[174:177], v1, v1 op_sel_hi:[0,0,0]
	v_lshl_add_u64 v[68:69], s[50:51], 0, v[210:211]
	s_add_i32 m0, s17, 0xe000
	s_nop 0
	global_load_lds_dwordx4 v[68:69], off
	v_mfma_scale_f32_16x16x128_f8f6f4 v[170:173], v[10:17], v[42:49], v[170:173], v1, v1 op_sel_hi:[0,0,0]
	s_mov_b32 m0, s19
	v_lshl_add_u64 v[68:69], s[52:53], 0, v[200:201]
	global_load_lds_dwordx4 v[68:69], off
	v_mfma_scale_f32_16x16x128_f8f6f4 v[166:169], v[2:9], v[42:49], v[166:169], v1, v1 op_sel_hi:[0,0,0]
	v_lshl_add_u64 v[212:213], s[52:53], 0, v[204:205]
	s_mov_b32 m0, s33
	v_lshl_add_u64 v[68:69], v[68:69], 0, s[4:5]
	global_load_lds_dwordx4 v[212:213], off
	v_mfma_scale_f32_16x16x128_f8f6f4 v[154:157], v[10:17], v[50:57], v[154:157], v1, v1 op_sel_hi:[0,0,0]
	s_mov_b32 m0, s45
	s_nop 0
	global_load_lds_dwordx4 v[68:69], off
	v_mfma_scale_f32_16x16x128_f8f6f4 v[150:153], v[2:9], v[50:57], v[150:153], v1, v1 op_sel_hi:[0,0,0]
	v_lshl_add_u64 v[68:69], v[212:213], 0, s[4:5]
	s_mov_b32 m0, s47
	v_lshl_add_u64 v[212:213], s[54:55], 0, v[202:203]
	global_load_lds_dwordx4 v[68:69], off
	v_mfma_scale_f32_16x16x128_f8f6f4 v[138:141], v[10:17], v[58:65], v[138:141], v1, v1 op_sel_hi:[0,0,0]
	v_lshl_add_u64 v[68:69], s[54:55], 0, v[198:199]
	s_mov_b32 m0, s17
	s_nop 0
	global_load_lds_dwordx4 v[68:69], off
	v_mfma_scale_f32_16x16x128_f8f6f4 v[134:137], v[2:9], v[58:65], v[134:137], v1, v1 op_sel_hi:[0,0,0]
	s_mov_b32 m0, s58
	s_nop 0
	global_load_lds_dwordx4 v[212:213], off
	s_setprio 0
	s_barrier
	s_andn2_b64 vcc, exec, s[48:49]
	s_cbranch_vccnz .Lp8t_halfskip_a
	ds_read_b128 v[58:61], v223 offset:16384
	ds_read_b128 v[62:65], v223 offset:17408
	ds_read_b128 v[50:53], v223 offset:18432
	ds_read_b128 v[54:57], v223 offset:19456
	ds_read_b128 v[42:45], v223 offset:20480
	ds_read_b128 v[46:49], v223 offset:21504
	ds_read_b128 v[34:37], v223 offset:22528
	ds_read_b128 v[38:41], v223 offset:23552

.Lp8t_903:
	s_add_u32 s56, s52, 0x40000
	s_addc_u32 s57, s53, 0
	s_barrier
	ds_read_b64_tr_b16 v[26:27], v215 offset:0
	ds_read_b64_tr_b16 v[28:29], v215 offset:1024
	ds_read_b64_tr_b16 v[30:31], v215 offset:8192
	ds_read_b64_tr_b16 v[32:33], v215 offset:9216
	ds_read_b64_tr_b16 v[18:19], v219 offset:0
	ds_read_b64_tr_b16 v[20:21], v219 offset:1024
	ds_read_b64_tr_b16 v[22:23], v219 offset:8192
	ds_read_b64_tr_b16 v[24:25], v219 offset:9216
	ds_read_b64_tr_b16 v[10:11], v216 offset:0
	ds_read_b64_tr_b16 v[12:13], v216 offset:1024
	ds_read_b64_tr_b16 v[14:15], v216 offset:8192
	ds_read_b64_tr_b16 v[16:17], v216 offset:9216
	ds_read_b64_tr_b16 v[2:3], v220 offset:0
	ds_read_b64_tr_b16 v[4:5], v220 offset:1024
	ds_read_b64_tr_b16 v[6:7], v220 offset:8192
	ds_read_b64_tr_b16 v[8:9], v220 offset:9216
	s_add_u32 s54, s54, 0x40000
	s_addc_u32 s55, s55, 0
	ds_read_b128 v[34:37], v223 offset:32768
	ds_read_b128 v[38:41], v223 offset:33792
	ds_read_b128 v[42:45], v223 offset:34816
	ds_read_b128 v[46:49], v223 offset:35840
	ds_read_b128 v[50:53], v223 offset:36864
	ds_read_b128 v[54:57], v223 offset:37888
	ds_read_b128 v[58:61], v223 offset:38912
	ds_read_b128 v[62:65], v223 offset:39936
	s_waitcnt vmcnt(6)
	s_waitcnt lgkmcnt(0)
	s_barrier
	s_setprio 1
	s_waitcnt lgkmcnt(0)
	v_mfma_scale_f32_16x16x128_f8f6f4 v[194:197], v[26:33], v[34:41], v[194:197], v1, v1 op_sel_hi:[0,0,0]
	v_mfma_scale_f32_16x16x128_f8f6f4 v[190:193], v[18:25], v[34:41], v[190:193], v1, v1 op_sel_hi:[0,0,0]
	v_mfma_scale_f32_16x16x128_f8f6f4 v[186:189], v[26:33], v[42:49], v[186:189], v1, v1 op_sel_hi:[0,0,0]
	v_mfma_scale_f32_16x16x128_f8f6f4 v[182:185], v[18:25], v[42:49], v[182:185], v1, v1 op_sel_hi:[0,0,0]
	s_mov_b32 m0, s59
	v_lshl_add_u64 v[226:227], s[54:55], 0, v[198:199]
	global_load_lds_dwordx4 v[226:227], off
	v_mfma_scale_f32_16x16x128_f8f6f4 v[162:165], v[26:33], v[50:57], v[162:165], v1, v1 op_sel_hi:[0,0,0]
	v_mfma_scale_f32_16x16x128_f8f6f4 v[158:161], v[18:25], v[50:57], v[158:161], v1, v1 op_sel_hi:[0,0,0]
	v_mfma_scale_f32_16x16x128_f8f6f4 v[146:149], v[26:33], v[58:65], v[146:149], v1, v1 op_sel_hi:[0,0,0]
	v_mfma_scale_f32_16x16x128_f8f6f4 v[142:145], v[18:25], v[58:65], v[142:145], v1, v1 op_sel_hi:[0,0,0]
	s_setprio 0
	s_setprio 1
	v_mfma_scale_f32_16x16x128_f8f6f4 v[178:181], v[10:17], v[34:41], v[178:181], v1, v1 op_sel_hi:[0,0,0]
	v_mfma_scale_f32_16x16x128_f8f6f4 v[174:177], v[2:9], v[34:41], v[174:177], v1, v1 op_sel_hi:[0,0,0]
	v_lshl_add_u64 v[226:227], s[54:55], 0, v[202:203]
	s_mov_b32 m0, s60
	s_nop 0
	global_load_lds_dwordx4 v[226:227], off
	v_mfma_scale_f32_16x16x128_f8f6f4 v[170:173], v[10:17], v[42:49], v[170:173], v1, v1 op_sel_hi:[0,0,0]
	v_lshl_add_u64 v[226:227], s[56:57], 0, v[200:201]
	s_add_i32 m0, s17, 0x18000
	s_nop 0
	global_load_lds_dwordx4 v[226:227], off
	v_mfma_scale_f32_16x16x128_f8f6f4 v[166:169], v[2:9], v[42:49], v[166:169], v1, v1 op_sel_hi:[0,0,0]
	s_add_i32 m0, s17, 0x1a000
	v_lshl_add_u64 v[226:227], s[56:57], 0, v[204:205]
	global_load_lds_dwordx4 v[226:227], off
	v_mfma_scale_f32_16x16x128_f8f6f4 v[154:157], v[10:17], v[50:57], v[154:157], v1, v1 op_sel_hi:[0,0,0]
	s_add_u32 s52, s52, 0x40100
	s_addc_u32 s53, s53, 0
	v_lshl_add_u64 v[226:227], s[52:53], 0, v[200:201]
	s_add_i32 m0, s17, 0x1c000
	v_lshl_add_u64 v[68:69], v[68:69], 0, s[12:13]
	global_load_lds_dwordx4 v[226:227], off
	v_mfma_scale_f32_16x16x128_f8f6f4 v[150:153], v[2:9], v[50:57], v[150:153], v1, v1 op_sel_hi:[0,0,0]
	v_lshl_add_u64 v[226:227], s[52:53], 0, v[204:205]
	s_add_i32 m0, s17, 0x1e000
	s_nop 0
	global_load_lds_dwordx4 v[226:227], off
	v_mfma_scale_f32_16x16x128_f8f6f4 v[138:141], v[10:17], v[58:65], v[138:141], v1, v1 op_sel_hi:[0,0,0]
	s_mov_b32 m0, s62
	s_nop 0
	global_load_lds_dwordx4 v[68:69], off
	v_mfma_scale_f32_16x16x128_f8f6f4 v[134:137], v[2:9], v[58:65], v[134:137], v1, v1 op_sel_hi:[0,0,0]
	v_lshl_add_u64 v[68:69], v[212:213], 0, s[12:13]
	s_mov_b32 m0, s63
	s_nop 0
	global_load_lds_dwordx4 v[68:69], off
	s_setprio 0
	s_barrier
	s_and_b64 vcc, exec, s[2:3]
	s_cbranch_vccnz .Lp8t_halfskip_b
	ds_read_b128 v[58:61], v223 offset:49152
	ds_read_b128 v[62:65], v223 offset:50176
	ds_read_b128 v[50:53], v223 offset:51200
	ds_read_b128 v[54:57], v223 offset:52224
	ds_read_b128 v[42:45], v223 offset:53248
	ds_read_b128 v[46:49], v223 offset:54272
	ds_read_b128 v[34:37], v223 offset:55296
	ds_read_b128 v[38:41], v223 offset:56320
